# rwkv state scan: chunk images prefetched two chunks ahead into two alternating register sets, single counted vmcnt(8) at the chunk head (no wait on the previous chunk's y store or on a one-chunk-old l
# baseline (speedup 1.0000x reference)
; __device__ __forceinline__ void rwkv_state_phase(LAS unsigned char* lds, const unsigned char* img, bf16_t* y_, const RwScan& a_, const int vcu, const int G, const int tid0_) {
;     ...
;         q0a = q0b = q1a = q1b = q2a = q2b = q3 = (u32x4){0u, 0u, 0u, 0u};
;         ST_FETCH(0);
.LBB0_743:
	s_or_b64 exec, exec, s[10:11]
	s_add_u32 s2, s2, 0x7100
	s_addc_u32 s3, s3, 0
	v_lshl_add_u64 v[4:5], s[2:3], 0, v[70:71]
	s_nop 0
	v_add_co_u32_e32 v8, vcc, 0x1000, v4
	s_nop 0
	s_nop 0
	v_addc_co_u32_e32 v9, vcc, 0, v5, vcc
	global_load_dwordx4 v[118:121], v[4:5], off
	global_load_dwordx4 v[122:125], v[8:9], off
	v_add_co_u32_e32 v8, vcc, 0x5000, v4
	s_nop 1
	v_addc_co_u32_e32 v9, vcc, 0, v5, vcc
	s_nop 0
	v_add_co_u32_e32 v10, vcc, 0x6000, v4
	s_nop 0
	s_nop 0
	v_addc_co_u32_e32 v11, vcc, 0, v5, vcc
	global_load_dwordx4 v[126:129], v[8:9], off
	global_load_dwordx4 v[130:133], v[10:11], off
	v_add_co_u32_e32 v8, vcc, 0x2000, v4
	s_nop 1
	v_addc_co_u32_e32 v9, vcc, 0, v5, vcc
	v_add_co_u32_e32 v4, vcc, 0x3000, v4
	s_nop 1
	v_addc_co_u32_e32 v5, vcc, 0, v5, vcc
	global_load_dwordx4 v[134:137], v[8:9], off
	global_load_dwordx4 v[138:141], v[4:5], off
	s_and_saveexec_b64 s[10:11], s[4:5]
	s_xor_b64 s[10:11], exec, s[10:11]
	s_cbranch_execz .Lrw2p_741
	v_mov_b32_e32 v4, v3
	v_mov_b32_e32 v5, v3
	v_mov_b32_e32 v2, v3
	v_mov_b64_e32 v[144:145], v[4:5]
	v_mov_b64_e32 v[142:143], v[2:3]
	s_and_saveexec_b64 s[28:29], s[6:7]
	s_cbranch_execz .Lrw2p_740
	v_lshl_add_u64 v[4:5], s[2:3], 0, v[72:73]
	v_add_co_u32_e32 v4, vcc, 0x6000, v4
	s_nop 1
	v_addc_co_u32_e32 v5, vcc, 0, v5, vcc
	global_load_dwordx4 v[142:145], v[4:5], off offset:2048

.Lrw2p_741:
	s_andn2_saveexec_b64 s[10:11], s[10:11]
	s_cbranch_execz .Lrw2p_743
	v_lshl_add_u64 v[4:5], s[2:3], 0, v[74:75]
	s_lshl_b32 s92, s34, 6
	v_lshl_add_u64 v[4:5], v[4:5], 0, s[92:93]
	v_lshl_add_u64 v[4:5], v[4:5], 0, v[76:77]
	v_add_co_u32_e32 v4, vcc, 0x4000, v4
	s_nop 1
	v_addc_co_u32_e32 v5, vcc, 0, v5, vcc
	global_load_dwordx4 v[142:145], v[4:5], off

; #define LAS __attribute__((address_space(3)))
; __device__ __forceinline__ void rwkv_state_phase(LAS unsigned char* lds, const unsigned char* img, bf16_t* y_, const RwScan& a_, const int vcu, const int G, const int tid0_) {
;     ...
;             if (wave < 4) {
;                 { const int o_ = (tid >> 3) * 144 + (tid & 7) * 16; *(LAS u32x4*)(lb + SK_AT + o_) = q0a; *(LAS u32x4*)(lb + SK_RT + o_) = q0b; }
;                 { const int idx = tid & 127, o_ = (tid >> 7) * 2560 + (idx >> 2) * 80 + (idx & 3) * 16; *(LAS u32x4*)(lb + SK_NAK + o_) = q1a; *(LAS u32x4*)(lb + SK_MKR + o_) = q1b; }
;                 { const int o_ = (tid >> 2) * 80 + (tid & 3) * 16; *(LAS u32x4*)(lb + SK_BH + o_) = q2a; *(LAS u32x4*)(lb + SK_KH + o_) = q2b; }
;                 if (tid < 128) { const int t_ = tid >> 2, i0_ = 8 * (tid & 3); const unsigned wv_[4] = {q3.x, q3.y, q3.z, q3.w};
; #pragma unroll
;                     for (int e = 0; e < 4; ++e) { Vi[(i0_ + 2 * e) * P32 + t_] = (bf16_t)(wv_[e] & 0xffffu); Vi[(i0_ + 2 * e + 1) * P32 + t_] = (bf16_t)(wv_[e] >> 16); } }
;                 else if (tid < 144) *(LAS u32x4*)(lb + SK_PL + (tid - 128) * 16) = q3;
;             }
;     ...
;             {
;                 const int mt = wave >> 1, nt = wave & 1;
;                 const f32x4 pl = *(const LAS f32x4*)(PL + 16 * mt + 4 * fq);
;                 Sacc = __builtin_amdgcn_mfma_f32_16x16x32_bf16(ldfrag(BhT, P32, 16 * mt + fr, 8 * fq), ldfrag(Ui, P32, 16 * nt + fr, 8 * fq), Sacc, 0, 0, 0);
;                 Sacc = __builtin_amdgcn_mfma_f32_16x16x32_bf16(ldfrag(KhT, P32, 16 * mt + fr, 8 * fq), ldfrag(Vi, P32, 16 * nt + fr, 8 * fq), Sacc, 0, 0, 0);
;                 Sacc = Sacc * pl;
;             }
.LBB0_745:
	s_and_b32 s10, s58, 0x3c0
	s_lshl_b32 s63, s31, 11
	s_lshl_b32 s2, s33, 1
	s_add_u32 s2, s43, s2
	s_addc_u32 s3, s44, 0
	s_lshl_b32 s11, s34, 6
	s_add_u32 s11, s2, s11
	s_addc_u32 s28, s3, 0
	s_lshl_b64 s[2:3], s[18:19], 1
	s_add_u32 s2, s11, s2
	v_cndmask_b32_e64 v2, 0, 1, s[22:23]
	s_addc_u32 s3, s28, s3
	s_add_i32 s28, s30, s10
	v_lshlrev_b32_e32 v2, 6, v2
	s_mul_hi_i32 s29, s28, 0x7100
	s_mul_i32 s30, s28, 0x7100
	v_mul_f32_e32 v62, 0, v6
	v_or_b32_e32 v4, s30, v2
	v_mov_b32_e32 v5, s29
	v_mov_b32_e32 v6, v3
	s_waitcnt vmcnt(30)
	v_mov_b32_e32 v7, v3
	s_waitcnt vmcnt(29)
	v_mov_b32_e32 v8, v3
	s_waitcnt vmcnt(28)
	v_mov_b32_e32 v9, v3
	s_waitcnt vmcnt(27)
	v_mov_b32_e32 v10, v3
	s_waitcnt vmcnt(26)
	v_mov_b32_e32 v11, v3
	s_waitcnt vmcnt(25)
	v_mov_b32_e32 v12, v3
	s_waitcnt vmcnt(24)
	v_mov_b32_e32 v13, v3
	s_waitcnt vmcnt(23)
	v_mov_b32_e32 v14, v3
	s_waitcnt vmcnt(22)
	v_mov_b32_e32 v15, v3
	s_waitcnt vmcnt(21)
	v_mov_b32_e32 v16, v3
	s_waitcnt vmcnt(20)
	v_mov_b32_e32 v17, v3
	s_waitcnt vmcnt(19)
	v_mov_b32_e32 v18, v3
	s_waitcnt vmcnt(18)
	v_mov_b32_e32 v19, v3
	s_waitcnt vmcnt(17)
	v_mov_b32_e32 v20, v3
	s_waitcnt vmcnt(16)
	v_mov_b32_e32 v21, v3
	s_waitcnt vmcnt(15)
	v_mov_b32_e32 v22, v3
	s_waitcnt vmcnt(14)
	v_mov_b32_e32 v23, v3
	s_waitcnt vmcnt(13)
	v_mov_b32_e32 v24, v3
	s_waitcnt vmcnt(12)
	v_mov_b32_e32 v25, v3
	s_waitcnt vmcnt(11)
	v_mov_b32_e32 v26, v3
	s_waitcnt vmcnt(10)
	v_mov_b32_e32 v27, v3
	s_waitcnt vmcnt(9)
	v_mov_b32_e32 v28, v3
	s_waitcnt vmcnt(8)
	v_mov_b32_e32 v29, v3
	s_waitcnt vmcnt(7)
	v_mov_b32_e32 v30, v3
	s_waitcnt vmcnt(6)
	v_mov_b32_e32 v31, v3
	s_waitcnt vmcnt(5)
	v_mov_b32_e32 v32, v3
	s_waitcnt vmcnt(4)
	v_mov_b32_e32 v33, v3
	v_lshl_add_u64 v[90:91], v[84:85], 0, v[4:5]
	v_mov_b32_e32 v2, v3
	v_mov_b32_e32 v4, v3
	v_mov_b32_e32 v5, v3
	v_mov_b32_e32 v63, 0
	s_waitcnt vmcnt(0)
	v_mov_b64_e32 v[36:37], v[32:33]
	s_or_b32 s33, s54, s63
	v_mad_i64_i32 v[88:89], s[10:11], s28, v246, v[82:83]
	v_mad_i64_i32 v[92:93], s[10:11], s28, v246, v[86:87]
	s_mov_b32 s64, 0
	s_mov_b64 s[30:31], 0
	s_mov_b64 s[28:29], 0x7100
	s_mov_b32 s62, s53
	v_mov_b64_e32 v[34:35], v[30:31]
	v_mov_b64_e32 v[32:33], v[28:29]
	v_mov_b64_e32 v[30:31], v[26:27]
	v_mov_b64_e32 v[28:29], v[24:25]
	v_mov_b64_e32 v[26:27], v[22:23]
	v_mov_b64_e32 v[24:25], v[20:21]
	v_mov_b64_e32 v[22:23], v[18:19]
	v_mov_b64_e32 v[20:21], v[16:17]
	v_mov_b64_e32 v[18:19], v[14:15]
	v_mov_b64_e32 v[16:17], v[12:13]
	v_mov_b64_e32 v[14:15], v[10:11]
	v_mov_b64_e32 v[12:13], v[8:9]
	v_mov_b64_e32 v[10:11], v[6:7]
	v_mov_b64_e32 v[8:9], v[4:5]
	v_mov_b64_e32 v[6:7], v[2:3]
	v_mov_b32_e32 v64, v63
	v_mov_b32_e32 v65, v63
	s_branch .LBB0_747
.LBB0_746:
	s_lshl_b32 s34, s18, 2
	s_add_i32 s34, s65, s34
	v_lshlrev_b32_e32 v2, 1, v2
	v_lshlrev_b32_e32 v5, 1, v5
	v_lshl_add_u32 v79, v97, 2, s34
	v_lshlrev_b32_e32 v4, 1, v4
	v_add3_u32 v2, s65, v2, v5
	v_add3_u32 v114, 0, v4, v5
	v_add3_u32 v115, s65, v4, v5
	ds_read_b128 v[94:97], v79 offset:41984
	ds_read_b128 v[98:101], v2 offset:31744
	ds_read_b128 v[102:105], v114 offset:29184
	ds_read_b128 v[160:163], v2 offset:36864
	ds_read_b128 v[164:167], v115 offset:24064
	s_add_i32 s33, s33, 32
	s_waitcnt lgkmcnt(2)
	v_mfma_f32_16x16x32_bf16 v[62:65], v[98:101], v[102:105], v[62:65]
	s_add_u32 s28, s28, 0x7100
	s_waitcnt lgkmcnt(0)
	v_mfma_f32_16x16x32_bf16 v[62:65], v[160:163], v[164:167], v[62:65]
	s_addc_u32 s29, s29, 0
	s_add_i32 s64, s64, 1
	s_cmp_eq_u32 s28, 0x1c4000
	s_nop 4
	v_pk_mul_f32 v[64:65], v[96:97], v[64:65]
	v_pk_mul_f32 v[62:63], v[94:95], v[62:63]
	s_cbranch_scc1 .LBB0_806
.LBB0_747:
	s_bitcmp1_b32 s64, 0
	s_cselect_b32 s10, 0xa500, 0
	v_mov_b32_e32 v2, v1
	s_and_b64 vcc, exec, s[8:9]
	s_add_i32 s65, s10, 0
	s_cbranch_vccnz .LBB0_755
	s_waitcnt vmcnt(8)
	s_bitcmp1_b32 s64, 0
	s_cbranch_scc1 .Lrw2_head_odd
	v_lshrrev_b32_e32 v4, 3, v2
	v_mul_lo_u32 v5, v4, s67
	v_lshlrev_b32_e32 v4, 4, v2
	v_and_b32_e32 v79, 0x70, v4
	v_add3_u32 v5, v5, v79, s65
	ds_write_b128 v5, v[42:45]
	ds_write_b128 v5, v[46:49] offset:4608
	v_lshrrev_b32_e32 v5, 7, v2
	s_movk_i32 s10, 0xa00
	v_mul_lo_u32 v5, v5, s10
	v_bfe_u32 v79, v2, 2, 5
	v_mul_u32_u24_e32 v79, 0x50, v79
	v_and_or_b32 v5, v4, 48, v5
	v_add3_u32 v5, v5, v79, s65
	ds_write_b128 v5, v[50:53] offset:13824
	ds_write_b128 v5, v[54:57] offset:18944
	v_ashrrev_i32_e32 v5, 2, v2
	v_and_b32_e32 v79, 3, v2
	v_mul_lo_u32 v81, v5, s66
	v_lshlrev_b32_e32 v94, 4, v79
	s_movk_i32 s10, 0x7f
	v_add3_u32 v81, v81, v94, s65
	v_cmp_lt_i32_e32 vcc, s10, v2
	ds_write_b128 v81, v[58:61] offset:31744
	ds_write_b128 v81, v[66:69] offset:36864
	s_and_saveexec_b64 s[10:11], vcc
	s_xor_b64 s[10:11], exec, s[10:11]
	s_cbranch_execz .LBB0_752
	v_cmp_gt_u32_e32 vcc, s67, v2
	s_and_saveexec_b64 s[34:35], vcc
	v_add_u32_e32 v4, s65, v4
	ds_write_b128 v4, v[38:41] offset:39936
	s_or_b64 exec, exec, s[34:35]
.LBB0_752:
	s_andn2_saveexec_b64 s[10:11], s[10:11]
	s_cbranch_execz .LBB0_754
	v_mul_u32_u24_e32 v4, 0x280, v79
	v_lshlrev_b32_e32 v5, 1, v5
	v_add3_u32 v4, s65, v4, v5
	ds_write_b16 v4, v38 offset:24064
	ds_write_b16_d16_hi v4, v38 offset:24144
	ds_write_b16 v4, v39 offset:24224
	ds_write_b16_d16_hi v4, v39 offset:24304
	ds_write_b16 v4, v40 offset:24384
	ds_write_b16_d16_hi v4, v40 offset:24464
	ds_write_b16 v4, v41 offset:24544
	ds_write_b16_d16_hi v4, v41 offset:24624
	s_branch .LBB0_754
.Lrw2_head_odd:
	v_lshrrev_b32_e32 v4, 3, v2
	v_mul_lo_u32 v5, v4, s67
	v_lshlrev_b32_e32 v4, 4, v2
	v_and_b32_e32 v79, 0x70, v4
	v_add3_u32 v5, v5, v79, s65
	ds_write_b128 v5, v[118:121]
	ds_write_b128 v5, v[122:125] offset:4608
	v_lshrrev_b32_e32 v5, 7, v2
	s_movk_i32 s10, 0xa00
	v_mul_lo_u32 v5, v5, s10
	v_bfe_u32 v79, v2, 2, 5
	v_mul_u32_u24_e32 v79, 0x50, v79
	v_and_or_b32 v5, v4, 48, v5
	v_add3_u32 v5, v5, v79, s65
	ds_write_b128 v5, v[126:129] offset:13824
	ds_write_b128 v5, v[130:133] offset:18944
	v_ashrrev_i32_e32 v5, 2, v2
	v_and_b32_e32 v79, 3, v2
	v_mul_lo_u32 v81, v5, s66
	v_lshlrev_b32_e32 v94, 4, v79
	s_movk_i32 s10, 0x7f
	v_add3_u32 v81, v81, v94, s65
	v_cmp_lt_i32_e32 vcc, s10, v2
	ds_write_b128 v81, v[134:137] offset:31744
	ds_write_b128 v81, v[138:141] offset:36864
	s_and_saveexec_b64 s[10:11], vcc
	s_xor_b64 s[10:11], exec, s[10:11]
	s_cbranch_execz .Lrw2h_752
	v_cmp_gt_u32_e32 vcc, s67, v2
	s_and_saveexec_b64 s[34:35], vcc
	v_add_u32_e32 v4, s65, v4
	ds_write_b128 v4, v[142:145] offset:39936
	s_or_b64 exec, exec, s[34:35]
.Lrw2h_752:
	s_andn2_saveexec_b64 s[10:11], s[10:11]
	s_cbranch_execz .LBB0_754
	v_mul_u32_u24_e32 v4, 0x280, v79
	v_lshlrev_b32_e32 v5, 1, v5
	v_add3_u32 v4, s65, v4, v5
	ds_write_b16 v4, v142 offset:24064
	ds_write_b16_d16_hi v4, v142 offset:24144
	ds_write_b16 v4, v143 offset:24224
	ds_write_b16_d16_hi v4, v143 offset:24304
	ds_write_b16 v4, v144 offset:24384
	ds_write_b16_d16_hi v4, v144 offset:24464
	ds_write_b16 v4, v145 offset:24544
	ds_write_b16_d16_hi v4, v145 offset:24624

; #define LAS __attribute__((address_space(3)))
; __device__ __forceinline__ unsigned cvt_pk_bf16(float lo, float hi) { const f32x2 v = {lo, hi}; const bf16x2_t b = __builtin_convertvector(v, bf16x2_t); return __builtin_bit_cast(unsigned, b); }
; __device__ __forceinline__ void rwkv_state_phase(LAS unsigned char* lds, const unsigned char* img, bf16_t* y_, const RwScan& a_, const int vcu, const int G, const int tid0_) {
;     ...
;             { const int mt = wave >> 1, nt = wave & 1; u32x2 o; o.x = cvt_pk_bf16(Sacc[0], Sacc[1]); o.y = cvt_pk_bf16(Sacc[2], Sacc[3]);
;               *(LAS u32x2*)(S0 + (16 * nt + fr) * P64 + 16 * mt + 4 * fq) = o; }
;             __syncthreads();
;             if (ch + 1 < SEQ / 32) ST_FETCH(ch + 1);
.LBB0_755:
	v_and_b32_e32 v81, 15, v2
	v_bfe_u32 v96, v2, 4, 2
	v_or_b32_e32 v95, s54, v81
	v_mov_b32_e32 v2, s65
	v_mad_u32_u24 v2, v95, s67, v2
	s_lshl_b32 s10, s18, 1
	v_lshlrev_b32_e32 v79, 3, v96
	v_cvt_pk_bf16_f32 v4, v62, v63
	v_cvt_pk_bf16_f32 v5, v64, v65
	v_add3_u32 v94, v2, s10, v79
	s_and_b64 vcc, exec, s[8:9]
	ds_write_b64 v94, v[4:5] offset:9216
	s_waitcnt lgkmcnt(0)
	s_barrier
	s_cbranch_vccnz .LBB0_763
	s_cmp_eq_u32 s28, 0x1bcf00
	s_cbranch_scc1 .LBB0_763
	s_bitcmp1_b32 s64, 0
	s_cbranch_scc1 .Lrw2_fetch_odd
	v_lshl_add_u64 v[4:5], v[88:89], 0, s[28:29]
	s_nop 0
	v_add_co_u32_e32 v42, vcc, 0x39507000, v4
	s_nop 1
	v_addc_co_u32_e32 v43, vcc, 0, v5, vcc
	s_nop 0
	v_add_co_u32_e32 v46, vcc, 0x39508000, v4
	s_nop 1
	v_addc_co_u32_e32 v47, vcc, 0, v5, vcc
	s_nop 0
	v_add_co_u32_e32 v50, vcc, 0x3950c000, v4
	global_load_dwordx4 v[42:45], v[42:43], off offset:256
	s_nop 0
	global_load_dwordx4 v[46:49], v[46:47], off offset:256
	v_addc_co_u32_e32 v51, vcc, 0, v5, vcc
	s_nop 0
	v_add_co_u32_e32 v54, vcc, 0x3950d000, v4
	s_nop 1
	v_addc_co_u32_e32 v55, vcc, 0, v5, vcc
	s_nop 0
	v_add_co_u32_e32 v58, vcc, 0x39509000, v4
	global_load_dwordx4 v[50:53], v[50:51], off offset:256
	s_nop 0
	global_load_dwordx4 v[54:57], v[54:55], off offset:256
	v_addc_co_u32_e32 v59, vcc, 0, v5, vcc
	v_add_co_u32_e32 v4, vcc, 0x3950a000, v4
	s_nop 1
	v_addc_co_u32_e32 v5, vcc, 0, v5, vcc
	global_load_dwordx4 v[58:61], v[58:59], off offset:256
	s_nop 0
	global_load_dwordx4 v[66:69], v[4:5], off offset:256
	s_and_saveexec_b64 s[10:11], s[4:5]
	s_xor_b64 s[10:11], exec, s[10:11]
	s_cbranch_execz .LBB0_760
	s_and_saveexec_b64 s[34:35], s[6:7]
	s_cbranch_execz .LBB0_759
	v_lshl_add_u64 v[4:5], v[92:93], 0, s[28:29]
	global_load_dwordx4 v[38:41], v[4:5], off

.LBB0_760:
	s_andn2_saveexec_b64 s[10:11], s[10:11]
	s_cbranch_execz .LBB0_762
	v_lshl_add_u64 v[4:5], v[90:91], 0, s[28:29]
	global_load_dwordx4 v[38:41], v[4:5], off
.LBB0_762:
	s_or_b64 exec, exec, s[10:11]
	s_branch .LBB0_763
.Lrw2_fetch_odd:
	v_lshl_add_u64 v[4:5], v[88:89], 0, s[28:29]
	s_nop 0
	v_add_co_u32_e32 v118, vcc, 0x39507000, v4
	s_nop 1
	v_addc_co_u32_e32 v119, vcc, 0, v5, vcc
	s_nop 0
	v_add_co_u32_e32 v122, vcc, 0x39508000, v4
	s_nop 1
	v_addc_co_u32_e32 v123, vcc, 0, v5, vcc
	s_nop 0
	v_add_co_u32_e32 v126, vcc, 0x3950c000, v4
	global_load_dwordx4 v[118:121], v[118:119], off offset:256
	s_nop 0
	global_load_dwordx4 v[122:125], v[122:123], off offset:256
	v_addc_co_u32_e32 v127, vcc, 0, v5, vcc
	s_nop 0
	v_add_co_u32_e32 v130, vcc, 0x3950d000, v4
	s_nop 1
	v_addc_co_u32_e32 v131, vcc, 0, v5, vcc
	s_nop 0
	v_add_co_u32_e32 v134, vcc, 0x39509000, v4
	global_load_dwordx4 v[126:129], v[126:127], off offset:256
	s_nop 0
	global_load_dwordx4 v[130:133], v[130:131], off offset:256
	v_addc_co_u32_e32 v135, vcc, 0, v5, vcc
	v_add_co_u32_e32 v4, vcc, 0x3950a000, v4
	s_nop 1
	v_addc_co_u32_e32 v5, vcc, 0, v5, vcc
	global_load_dwordx4 v[134:137], v[134:135], off offset:256
	s_nop 0
	global_load_dwordx4 v[138:141], v[4:5], off offset:256
	s_and_saveexec_b64 s[10:11], s[4:5]
	s_xor_b64 s[10:11], exec, s[10:11]
	s_cbranch_execz .Lrw2f_760
	s_and_saveexec_b64 s[34:35], s[6:7]
	s_cbranch_execz .Lrw2f_759
	v_lshl_add_u64 v[4:5], v[92:93], 0, s[28:29]
	global_load_dwordx4 v[142:145], v[4:5], off

.Lrw2f_760:
	s_andn2_saveexec_b64 s[10:11], s[10:11]
	s_cbranch_execz .Lrw2f_762
	v_lshl_add_u64 v[4:5], v[90:91], 0, s[28:29]
	global_load_dwordx4 v[142:145], v[4:5], off

; #define LAS __attribute__((address_space(3)))
; __device__ __forceinline__ void rwkv_state_phase(LAS unsigned char* lds, const unsigned char* img, bf16_t* y_, const RwScan& a_, const int vcu, const int G, const int tid0_) {
;     ...
;             if (wave < 4) {
;                 { const int o_ = (tid >> 3) * 144 + (tid & 7) * 16; *(LAS u32x4*)(lb + SK_AT + o_) = q0a; *(LAS u32x4*)(lb + SK_RT + o_) = q0b; }
;                 { const int idx = tid & 127, o_ = (tid >> 7) * 2560 + (idx >> 2) * 80 + (idx & 3) * 16; *(LAS u32x4*)(lb + SK_NAK + o_) = q1a; *(LAS u32x4*)(lb + SK_MKR + o_) = q1b; }
;                 { const int o_ = (tid >> 2) * 80 + (tid & 3) * 16; *(LAS u32x4*)(lb + SK_BH + o_) = q2a; *(LAS u32x4*)(lb + SK_KH + o_) = q2b; }
;                 if (tid < 128) { const int t_ = tid >> 2, i0_ = 8 * (tid & 3); const unsigned wv_[4] = {q3.x, q3.y, q3.z, q3.w};
; #pragma unroll
;                     for (int e = 0; e < 4; ++e) { Vi[(i0_ + 2 * e) * P32 + t_] = (bf16_t)(wv_[e] & 0xffffu); Vi[(i0_ + 2 * e + 1) * P32 + t_] = (bf16_t)(wv_[e] >> 16); } }
;                 else if (tid < 144) *(LAS u32x4*)(lb + SK_PL + (tid - 128) * 16) = q3;
;             }
.LBB0_806:
	v_mov_b32_e32 v2, v1
	s_and_b64 vcc, exec, s[8:9]
	s_cbranch_vccnz .LBB0_814
	s_waitcnt vmcnt(2)
	v_lshrrev_b32_e32 v4, 3, v2
	v_mul_lo_u32 v5, v4, s67
	v_lshlrev_b32_e32 v4, 4, v2
	v_and_b32_e32 v79, 0x70, v4
	v_add3_u32 v5, v5, v79, 0
	ds_write_b128 v5, v[118:121] offset:42240
	ds_write_b128 v5, v[122:125] offset:46848
	v_lshrrev_b32_e32 v5, 7, v2
	s_movk_i32 s28, 0xa00
	v_mul_lo_u32 v5, v5, s28
	v_bfe_u32 v118, v2, 2, 5
	v_mul_u32_u24_e32 v118, 0x50, v118
	v_and_or_b32 v5, v4, 48, v5
	v_add3_u32 v5, v5, v118, 0
	ds_write_b128 v5, v[126:129] offset:56064
	ds_write_b128 v5, v[130:133] offset:61184
	v_ashrrev_i32_e32 v5, 2, v2
	v_and_b32_e32 v118, 3, v2
	v_mul_lo_u32 v119, v5, s66
	v_lshlrev_b32_e32 v120, 4, v118
	v_add3_u32 v119, v119, v120, 0
	s_movk_i32 s28, 0x7f
	v_add_u32_e32 v120, 0x12100, v119
	v_add_u32_e32 v119, 0x13500, v119
	v_cmp_lt_i32_e32 vcc, s28, v2
	ds_write_b128 v120, v[134:137]
	ds_write_b128 v119, v[138:141]
	s_and_saveexec_b64 s[28:29], vcc
	s_xor_b64 s[28:29], exec, s[28:29]
	s_cbranch_execz .LBB0_811
	v_cmp_gt_u32_e32 vcc, s67, v2
	s_and_saveexec_b64 s[34:35], vcc
	s_cbranch_execz .LBB0_810
	v_readlane_b32 s33, v253, 57
	s_nop 1
	v_add_u32_e32 v4, s33, v4
	v_add_u32_e32 v4, 0xfffff800, v4
	ds_write_b128 v4, v[142:145]

; __device__ __forceinline__ void rwkv_state_phase(LAS unsigned char* lds, const unsigned char* img, bf16_t* y_, const RwScan& a_, const int vcu, const int G, const int tid0_) {
;     ...
;                 if (tid < 128) { const int t_ = tid >> 2, i0_ = 8 * (tid & 3); const unsigned wv_[4] = {q3.x, q3.y, q3.z, q3.w};
; #pragma unroll
;                     for (int e = 0; e < 4; ++e) { Vi[(i0_ + 2 * e) * P32 + t_] = (bf16_t)(wv_[e] & 0xffffu); Vi[(i0_ + 2 * e + 1) * P32 + t_] = (bf16_t)(wv_[e] >> 16); } }
.LBB0_811:
	s_andn2_saveexec_b64 s[28:29], s[28:29]
	s_cbranch_execz .LBB0_813
	v_mul_u32_u24_e32 v4, 0x280, v118
	v_lshlrev_b32_e32 v5, 1, v5
	v_readlane_b32 s33, v253, 58
	s_nop 1
	v_add3_u32 v4, s33, v4, v5
	ds_write_b16 v4, v142
	ds_write_b16_d16_hi v4, v142 offset:80
	ds_write_b16 v4, v143 offset:160
	ds_write_b16_d16_hi v4, v143 offset:240
	ds_write_b16 v4, v144 offset:320
	ds_write_b16_d16_hi v4, v144 offset:400
	ds_write_b16 v4, v145 offset:480
	ds_write_b16_d16_hi v4, v145 offset:560
